# phase 3 row work (latent norms + k_rope): 9 rows per wave on the 128 workgroups that run one scan unit fewer, all row loads in flight, wave reductions of 3 rows interleaved
# speedup vs baseline: 1.0051x; 1.0051x over previous
; DI void phase_l0_rows(const Params& p, int G, int bid) {
;     const int lane = threadIdx.x & 63, wave = threadIdx.x >> 6;
;     const bf16_t* Z = (const bf16_t*)(p.ws + WS_Z);
;     bf16_t* CQN = (bf16_t*)(p.ws + WS_CQN); bf16_t* CKVN = (bf16_t*)(p.ws + WS_CKVN); bf16_t* KR = (bf16_t*)(p.ws + WS_KR);
;     const f32x2* R0 = (const f32x2*)(p.ws + WS_ROPE0);
;     const bool wdeal = (G == 256);
;     const int nslot = NTOK / 8;
;     const int s_first = !wdeal ? bid : (bid < 128 ? bid : 128 + (bid - 128) * 4), s_cnt = !wdeal ? 1 : (bid < 128 ? 1 : 4), s_step = !wdeal ? G : 640;
;     for (int sb = s_first; sb < nslot; sb += s_step)
;     for (int sj = 0; sj < s_cnt && sb + sj < nslot; ++sj) {
;         const int row = (sb + sj) * 8 + wave;
;         const bf16_t* z = Z + (size_t)row * L0INP;
;         {
;             const u32x4 w = *(const u32x4*)(z + 8 * lane);
;             float v[8] = {bflo(w.x), bfhi(w.x), bflo(w.y), bfhi(w.y), bflo(w.z), bfhi(w.z), bflo(w.w), bfhi(w.w)};
;             float ss = 0.f;
; #pragma unroll
;             for (int j = 0; j < 8; ++j) ss += v[j] * v[j];
;             ss = wave_sum(ss);
;             const float r = rsqrtf(ss * (1.0f / 512.0f) + EPS);
;             const f32x4 g0 = *(const f32x4*)(p.in[12] + 8 * lane), g1 = *(const f32x4*)(p.in[12] + 8 * lane + 4);
;             u32x4 o; o.x = pk_bf16(v[0] * r * g0[0], v[1] * r * g0[1]); o.y = pk_bf16(v[2] * r * g0[2], v[3] * r * g0[3]);
;             o.z = pk_bf16(v[4] * r * g1[0], v[5] * r * g1[1]); o.w = pk_bf16(v[6] * r * g1[2], v[7] * r * g1[3]);
;             *(u32x4*)(CQN + (size_t)row * 512 + 8 * lane) = o;
;         }
;         {
;             const u32x2 w = *(const u32x2*)(z + 512 + 4 * lane);
;             float v[4] = {bflo(w.x), bfhi(w.x), bflo(w.y), bfhi(w.y)};
;             float ss = v[0] * v[0] + v[1] * v[1] + v[2] * v[2] + v[3] * v[3];
;             ss = wave_sum(ss);
;             const float r = rsqrtf(ss * (1.0f / 256.0f) + EPS);
;             const f32x4 g = *(const f32x4*)(p.in[14] + 4 * lane);
;             u32x2 o; o.x = pk_bf16(v[0] * r * g[0], v[1] * r * g[1]); o.y = pk_bf16(v[2] * r * g[2], v[3] * r * g[3]);
;             *(u32x2*)(CKVN + (size_t)row * 256 + 4 * lane) = o;
;         }
;         {
;             const float x = bf2f(z[768 + lane]);
;             const float xp = __shfl_xor(x, 16);
;             float o = x;
.LBB0_328:
	s_cmp_gt_i32 s24, 3
	s_cselect_b64 s[0:1], -1, 0
	s_cmp_lt_i32 s25, 4
	s_cselect_b64 s[2:3], -1, 0
	s_or_b64 s[0:1], s[0:1], s[2:3]
	s_and_b64 vcc, exec, s[0:1]
	s_cbranch_vccnz .LBB0_409
	s_cmpk_eq_i32 s23, 0x100
	s_cselect_b64 s[2:3], -1, 0
	s_cmpk_gt_i32 s22, 0x7f
	s_cselect_b64 s[0:1], -1, 0
	s_lshl_b32 s4, s22, 2
	s_and_b64 s[0:1], s[0:1], s[2:3]
	s_add_i32 s6, s4, 0xfffffe80
	s_and_b64 s[4:5], s[0:1], exec
	s_cselect_b32 s10, s6, s22
	s_cmpk_gt_i32 s10, 0x47f
	s_cbranch_scc1 .LBB0_336
	v_and_b32_e32 v1, 16, v0
	v_cmp_eq_u32_e64 s[4:5], 0, v1
	v_mbcnt_lo_u32_b32 v1, -1, 0
	v_mbcnt_hi_u32_b32 v14, -1, v1
	v_and_b32_e32 v1, 64, v14
	v_add_u32_e32 v15, 64, v1
	v_xor_b32_e32 v1, 32, v14
	v_cmp_lt_i32_e32 vcc, v1, v15
	v_xor_b32_e32 v17, 16, v14
	s_add_u32 s8, s50, 0x2660e000
	v_cndmask_b32_e32 v1, v14, v1, vcc
	v_cmp_lt_i32_e32 vcc, v17, v15
	s_addc_u32 s9, s51, 0
	s_add_u32 s6, s50, 0x88000
	v_cndmask_b32_e32 v17, v14, v17, vcc
	v_lshlrev_b32_e32 v22, 2, v17
	v_xor_b32_e32 v17, 8, v14
	v_cmp_lt_i32_e32 vcc, v17, v15
	s_addc_u32 s7, s51, 0
	v_and_b32_e32 v18, 63, v0
	v_cndmask_b32_e32 v17, v14, v17, vcc
	v_lshlrev_b32_e32 v23, 2, v17
	v_xor_b32_e32 v17, 4, v14
	v_cmp_lt_i32_e32 vcc, v17, v15
	v_mov_b32_e32 v3, 0
	s_and_b64 s[2:3], s[2:3], exec
	v_cndmask_b32_e32 v17, v14, v17, vcc
	v_lshlrev_b32_e32 v24, 2, v17
	v_xor_b32_e32 v17, 2, v14
	v_cmp_lt_i32_e32 vcc, v17, v15
	v_lshlrev_b32_e32 v12, 4, v18
	v_mov_b32_e32 v13, v3
	v_cndmask_b32_e32 v17, v14, v17, vcc
	v_readlane_b32 s68, v251, 16
	v_lshlrev_b32_e32 v25, 2, v17
	v_xor_b32_e32 v17, 1, v14
	v_lshlrev_b32_e32 v2, 3, v18
	v_lshl_add_u64 v[4:5], s[50:51], 0, v[12:13]
	s_mov_b64 s[2:3], 0x2b70e000
	v_lshlrev_b32_e32 v8, 1, v18
	v_mov_b32_e32 v9, v3
	v_readlane_b32 s72, v251, 20
	v_readlane_b32 s73, v251, 21
	v_readlane_b32 s76, v251, 24
	v_readlane_b32 s77, v251, 25
	v_readlane_b32 s80, v251, 28
	v_readlane_b32 s81, v251, 29
	v_cmp_lt_i32_e32 vcc, v17, v15
	s_cselect_b32 s11, 0x280, s23
	v_lshl_add_u64 v[4:5], v[4:5], 0, s[2:3]
	v_lshlrev_b32_e32 v16, 2, v18
	v_lshl_add_u64 v[6:7], s[50:51], 0, v[2:3]
	s_mov_b64 s[2:3], 0x2c00e000
	v_and_b32_e32 v20, 15, v0
	v_lshl_add_u64 v[8:9], s[50:51], 0, v[8:9]
	s_mov_b64 s[12:13], 0x2c48e000
	v_lshlrev_b32_e32 v10, 5, v18
	v_mov_b32_e32 v11, v3
	s_mov_b64 s[72:73], s[76:77]
	s_mov_b64 s[76:77], s[80:81]
	v_cndmask_b32_e32 v14, v14, v17, vcc
	v_lshl_add_u64 v[6:7], v[6:7], 0, s[2:3]
	v_cmp_gt_u32_e64 s[2:3], 32, v18
	v_lshl_add_u64 v[8:9], v[8:9], 0, s[12:13]
	v_lshl_add_u64 v[10:11], s[72:73], 0, v[10:11]
	v_lshl_add_u64 v[12:13], s[76:77], 0, v[12:13]
	v_lshlrev_b32_e32 v1, 2, v1
	v_lshlrev_b32_e32 v26, 2, v14
	v_lshl_or_b32 v27, s10, 3, v222
	s_lshl_b32 s12, s11, 3
	s_movk_i32 s13, 0x1800
	v_mov_b64_e32 v[14:15], s[8:9]
	v_lshlrev_b32_e32 v2, 1, v2
	v_mov_b32_e32 v28, 0x358637bd
	s_mov_b32 s14, 0x800000
	v_lshlrev_b32_e32 v16, 1, v16
	v_mov_b32_e32 v17, v3
	v_lshlrev_b32_e32 v18, 1, v18
	v_mov_b32_e32 v19, v3
	s_movk_i32 s15, 0x3ff
	v_lshlrev_b32_e32 v29, 3, v20
	v_readlane_b32 s69, v251, 17
	v_readlane_b32 s70, v251, 18
	v_readlane_b32 s71, v251, 19
	v_readlane_b32 s74, v251, 22
	v_readlane_b32 s75, v251, 23
	v_readlane_b32 s78, v251, 26
	v_readlane_b32 s79, v251, 27
	v_readlane_b32 s82, v251, 30
	v_readlane_b32 s83, v251, 31
	s_cmpk_lg_i32 s23, 0x100
	s_cbranch_scc1 .LBB0_332
	s_cmpk_lt_i32 s22, 0x80
	s_cbranch_scc1 .LBB0_336
	v_readfirstlane_b32 s17, v222
	s_sub_i32 s16, s22, 0x80
	s_mul_i32 s16, s16, 72
	s_add_i32 s16, s16, s17
	global_load_dwordx4 v[34:37], v[10:11], off
	global_load_dwordx4 v[38:41], v[10:11], off offset:16
	global_load_dwordx4 v[42:45], v[12:13], off
	s_add_i32 s18, s16, 0
	s_mul_i32 s19, s18, 0x1800
	s_add_u32 s84, s8, s19
	s_addc_u32 s85, s9, 0
	global_load_dwordx4 v[48:51], v2, s[84:85]
	global_load_dwordx2 v[52:53], v16, s[84:85] offset:1024
	global_load_ushort v56, v18, s[84:85] offset:1536
	s_cmpk_lt_u32 s18, 0x400
	s_cbranch_scc1 .Ll0r_nr0
	s_and_b32 s19, s18, 63
	s_bfe_u32 s30, s18, 0x50006
	s_xor_b32 s30, s30, 16
	v_mov_b32_e32 v54, s19
	v_mov_b32_e32 v55, s30
	v_cndmask_b32_e64 v54, v54, v55, s[2:3]
	v_lshl_or_b32 v54, v54, 7, v29
	global_load_dwordx2 v[54:55], v54, s[6:7]
.Ll0r_nr0:
	s_add_i32 s18, s16, 8
	s_mul_i32 s19, s18, 0x1800
	s_add_u32 s84, s8, s19
	s_addc_u32 s85, s9, 0
	global_load_dwordx4 v[58:61], v2, s[84:85]
	global_load_dwordx2 v[62:63], v16, s[84:85] offset:1024
	global_load_ushort v66, v18, s[84:85] offset:1536
	s_cmpk_lt_u32 s18, 0x400
	s_cbranch_scc1 .Ll0r_nr1
	s_and_b32 s19, s18, 63
	s_bfe_u32 s30, s18, 0x50006
	s_xor_b32 s30, s30, 16
	v_mov_b32_e32 v64, s19
	v_mov_b32_e32 v65, s30
	v_cndmask_b32_e64 v64, v64, v65, s[2:3]
	v_lshl_or_b32 v64, v64, 7, v29
	global_load_dwordx2 v[64:65], v64, s[6:7]
.Ll0r_nr1:
	s_add_i32 s18, s16, 16
	s_mul_i32 s19, s18, 0x1800
	s_add_u32 s84, s8, s19
	s_addc_u32 s85, s9, 0
	global_load_dwordx4 v[68:71], v2, s[84:85]
	global_load_dwordx2 v[72:73], v16, s[84:85] offset:1024
	global_load_ushort v76, v18, s[84:85] offset:1536
	s_cmpk_lt_u32 s18, 0x400
	s_cbranch_scc1 .Ll0r_nr2
	s_and_b32 s19, s18, 63
	s_bfe_u32 s30, s18, 0x50006
	s_xor_b32 s30, s30, 16
	v_mov_b32_e32 v74, s19
	v_mov_b32_e32 v75, s30
	v_cndmask_b32_e64 v74, v74, v75, s[2:3]
	v_lshl_or_b32 v74, v74, 7, v29
	global_load_dwordx2 v[74:75], v74, s[6:7]
.Ll0r_nr2:
	s_add_i32 s18, s16, 24
	s_mul_i32 s19, s18, 0x1800
	s_add_u32 s84, s8, s19
	s_addc_u32 s85, s9, 0
	global_load_dwordx4 v[78:81], v2, s[84:85]
	global_load_dwordx2 v[82:83], v16, s[84:85] offset:1024
	global_load_ushort v86, v18, s[84:85] offset:1536
	s_cmpk_lt_u32 s18, 0x400
	s_cbranch_scc1 .Ll0r_nr3
	s_and_b32 s19, s18, 63
	s_bfe_u32 s30, s18, 0x50006
	s_xor_b32 s30, s30, 16
	v_mov_b32_e32 v84, s19
	v_mov_b32_e32 v85, s30
	v_cndmask_b32_e64 v84, v84, v85, s[2:3]
	v_lshl_or_b32 v84, v84, 7, v29
	global_load_dwordx2 v[84:85], v84, s[6:7]
; DI unsigned pk_bf16(float lo, float hi) { f32x2 v = {lo, hi}; hbf16x2 r = __builtin_convertvector(v, hbf16x2); return __builtin_bit_cast(unsigned, r); }
; DI float bflo(unsigned w) { return __uint_as_float(w << 16); }
; DI float bfhi(unsigned w) { return __uint_as_float(w & 0xffff0000u); }
; DI float bf2f(bf16_t b) { return __uint_as_float(((unsigned)b) << 16); }
; DI float wave_sum(float v) {
; #pragma unroll
;     for (int o = 32; o > 0; o >>= 1) v += __shfl_xor(v, o);
;     return v;
; DI void phase_l0_rows(const Params& p, int G, int bid) {
;     ...
;             const u32x4 w = *(const u32x4*)(z + 8 * lane);
;             float v[8] = {bflo(w.x), bfhi(w.x), bflo(w.y), bfhi(w.y), bflo(w.z), bfhi(w.z), bflo(w.w), bfhi(w.w)};
;             float ss = 0.f;
; #pragma unroll
;             for (int j = 0; j < 8; ++j) ss += v[j] * v[j];
;             ss = wave_sum(ss);
;             const float r = rsqrtf(ss * (1.0f / 512.0f) + EPS);
;             const f32x4 g0 = *(const f32x4*)(p.in[12] + 8 * lane), g1 = *(const f32x4*)(p.in[12] + 8 * lane + 4);
;             u32x4 o; o.x = pk_bf16(v[0] * r * g0[0], v[1] * r * g0[1]); o.y = pk_bf16(v[2] * r * g0[2], v[3] * r * g0[3]);
;             o.z = pk_bf16(v[4] * r * g1[0], v[5] * r * g1[1]); o.w = pk_bf16(v[6] * r * g1[2], v[7] * r * g1[3]);
;             *(u32x4*)(CQN + (size_t)row * 512 + 8 * lane) = o;
;         }
;         {
;             const u32x2 w = *(const u32x2*)(z + 512 + 4 * lane);
;             float v[4] = {bflo(w.x), bfhi(w.x), bflo(w.y), bfhi(w.y)};
;             float ss = v[0] * v[0] + v[1] * v[1] + v[2] * v[2] + v[3] * v[3];
;             ss = wave_sum(ss);
;             const float r = rsqrtf(ss * (1.0f / 256.0f) + EPS);
;             const f32x4 g = *(const f32x4*)(p.in[14] + 4 * lane);
;             u32x2 o; o.x = pk_bf16(v[0] * r * g[0], v[1] * r * g[1]); o.y = pk_bf16(v[2] * r * g[2], v[3] * r * g[3]);
;             *(u32x2*)(CKVN + (size_t)row * 256 + 4 * lane) = o;
;         }
;         {
;             const float x = bf2f(z[768 + lane]);
;             const float xp = __shfl_xor(x, 16);
.Ll0r_nr3:
	s_add_i32 s18, s16, 32
	s_mul_i32 s19, s18, 0x1800
	s_add_u32 s84, s8, s19
	s_addc_u32 s85, s9, 0
	global_load_dwordx4 v[88:91], v2, s[84:85]
	global_load_dwordx2 v[92:93], v16, s[84:85] offset:1024
	global_load_ushort v96, v18, s[84:85] offset:1536
	s_cmpk_lt_u32 s18, 0x400
	s_cbranch_scc1 .Ll0r_nr4
	s_and_b32 s19, s18, 63
	s_bfe_u32 s30, s18, 0x50006
	s_xor_b32 s30, s30, 16
	v_mov_b32_e32 v94, s19
	v_mov_b32_e32 v95, s30
	v_cndmask_b32_e64 v94, v94, v95, s[2:3]
	v_lshl_or_b32 v94, v94, 7, v29
	global_load_dwordx2 v[94:95], v94, s[6:7]
.Ll0r_nr4:
	s_add_i32 s18, s16, 40
	s_mul_i32 s19, s18, 0x1800
	s_add_u32 s84, s8, s19
	s_addc_u32 s85, s9, 0
	global_load_dwordx4 v[98:101], v2, s[84:85]
	global_load_dwordx2 v[102:103], v16, s[84:85] offset:1024
	global_load_ushort v106, v18, s[84:85] offset:1536
	s_cmpk_lt_u32 s18, 0x400
	s_cbranch_scc1 .Ll0r_nr5
	s_and_b32 s19, s18, 63
	s_bfe_u32 s30, s18, 0x50006
	s_xor_b32 s30, s30, 16
	v_mov_b32_e32 v104, s19
	v_mov_b32_e32 v105, s30
	v_cndmask_b32_e64 v104, v104, v105, s[2:3]
	v_lshl_or_b32 v104, v104, 7, v29
	global_load_dwordx2 v[104:105], v104, s[6:7]
.Ll0r_nr5:
	s_add_i32 s18, s16, 48
	s_mul_i32 s19, s18, 0x1800
	s_add_u32 s84, s8, s19
	s_addc_u32 s85, s9, 0
	global_load_dwordx4 v[108:111], v2, s[84:85]
	global_load_dwordx2 v[112:113], v16, s[84:85] offset:1024
	global_load_ushort v116, v18, s[84:85] offset:1536
	s_cmpk_lt_u32 s18, 0x400
	s_cbranch_scc1 .Ll0r_nr6
	s_and_b32 s19, s18, 63
	s_bfe_u32 s30, s18, 0x50006
	s_xor_b32 s30, s30, 16
	v_mov_b32_e32 v114, s19
	v_mov_b32_e32 v115, s30
	v_cndmask_b32_e64 v114, v114, v115, s[2:3]
	v_lshl_or_b32 v114, v114, 7, v29
	global_load_dwordx2 v[114:115], v114, s[6:7]
.Ll0r_nr6:
	s_add_i32 s18, s16, 56
	s_mul_i32 s19, s18, 0x1800
	s_add_u32 s84, s8, s19
	s_addc_u32 s85, s9, 0
	global_load_dwordx4 v[118:121], v2, s[84:85]
	global_load_dwordx2 v[122:123], v16, s[84:85] offset:1024
	global_load_ushort v126, v18, s[84:85] offset:1536
	s_cmpk_lt_u32 s18, 0x400
	s_cbranch_scc1 .Ll0r_nr7
	s_and_b32 s19, s18, 63
	s_bfe_u32 s30, s18, 0x50006
	s_xor_b32 s30, s30, 16
	v_mov_b32_e32 v124, s19
	v_mov_b32_e32 v125, s30
	v_cndmask_b32_e64 v124, v124, v125, s[2:3]
	v_lshl_or_b32 v124, v124, 7, v29
	global_load_dwordx2 v[124:125], v124, s[6:7]
.Ll0r_nr7:
	s_add_i32 s18, s16, 64
	s_mul_i32 s19, s18, 0x1800
	s_add_u32 s84, s8, s19
	s_addc_u32 s85, s9, 0
	global_load_dwordx4 v[128:131], v2, s[84:85]
	global_load_dwordx2 v[132:133], v16, s[84:85] offset:1024
	global_load_ushort v136, v18, s[84:85] offset:1536
	s_cmpk_lt_u32 s18, 0x400
	s_cbranch_scc1 .Ll0r_nr8
	s_and_b32 s19, s18, 63
	s_bfe_u32 s30, s18, 0x50006
	s_xor_b32 s30, s30, 16
	v_mov_b32_e32 v134, s19
	v_mov_b32_e32 v135, s30
	v_cndmask_b32_e64 v134, v134, v135, s[2:3]
	v_lshl_or_b32 v134, v134, 7, v29
	global_load_dwordx2 v[134:135], v134, s[6:7]
.Ll0r_nr8:
	s_waitcnt vmcnt(0)
	v_lshlrev_b32_e32 v140, 16, v48
	v_and_b32_e32 v141, 0xffff0000, v48
	v_lshlrev_b32_e32 v142, 16, v49
	v_and_b32_e32 v143, 0xffff0000, v49
	v_lshlrev_b32_e32 v144, 16, v50
	v_and_b32_e32 v145, 0xffff0000, v50
	v_lshlrev_b32_e32 v146, 16, v51
	v_and_b32_e32 v147, 0xffff0000, v51
	v_lshlrev_b32_e32 v148, 16, v52
	v_and_b32_e32 v149, 0xffff0000, v52
	v_lshlrev_b32_e32 v150, 16, v53
	v_and_b32_e32 v151, 0xffff0000, v53
	v_lshlrev_b32_e32 v152, 16, v56
	v_pk_mul_f32 v[156:157], v[140:141], v[140:141]
	v_pk_mul_f32 v[158:159], v[142:143], v[142:143]
	v_add_f32_e32 v154, v156, v157
	v_add_f32_e32 v154, v158, v154
	v_pk_mul_f32 v[156:157], v[144:145], v[144:145]
	v_add_f32_e32 v154, v159, v154
	v_add_f32_e32 v154, v156, v154
	v_pk_mul_f32 v[158:159], v[146:147], v[146:147]
	v_add_f32_e32 v154, v157, v154
	v_add_f32_e32 v154, v158, v154
	v_add_f32_e32 v154, v159, v154
	v_pk_mul_f32 v[156:157], v[148:149], v[148:149]
	v_pk_mul_f32 v[158:159], v[150:151], v[150:151]
	v_add_f32_e32 v155, v156, v157
	v_add_f32_e32 v155, v158, v155
	v_add_f32_e32 v155, v159, v155
	v_lshlrev_b32_e32 v162, 16, v58
	v_and_b32_e32 v163, 0xffff0000, v58
	v_lshlrev_b32_e32 v164, 16, v59
	v_and_b32_e32 v165, 0xffff0000, v59
	v_lshlrev_b32_e32 v166, 16, v60
	v_and_b32_e32 v167, 0xffff0000, v60
	v_lshlrev_b32_e32 v168, 16, v61
	v_and_b32_e32 v169, 0xffff0000, v61
	v_lshlrev_b32_e32 v170, 16, v62
	v_and_b32_e32 v171, 0xffff0000, v62
	v_lshlrev_b32_e32 v172, 16, v63
	v_and_b32_e32 v173, 0xffff0000, v63
	v_lshlrev_b32_e32 v174, 16, v66
	v_pk_mul_f32 v[178:179], v[162:163], v[162:163]
	v_pk_mul_f32 v[180:181], v[164:165], v[164:165]
	v_add_f32_e32 v176, v178, v179
	v_add_f32_e32 v176, v180, v176
	v_pk_mul_f32 v[178:179], v[166:167], v[166:167]
	v_add_f32_e32 v176, v181, v176
	v_add_f32_e32 v176, v178, v176
	v_pk_mul_f32 v[180:181], v[168:169], v[168:169]
	v_add_f32_e32 v176, v179, v176
	v_add_f32_e32 v176, v180, v176
	v_add_f32_e32 v176, v181, v176
	v_pk_mul_f32 v[178:179], v[170:171], v[170:171]
	v_pk_mul_f32 v[180:181], v[172:173], v[172:173]
	v_add_f32_e32 v177, v178, v179
	v_add_f32_e32 v177, v180, v177
	v_add_f32_e32 v177, v181, v177
	v_lshlrev_b32_e32 v184, 16, v68
	v_and_b32_e32 v185, 0xffff0000, v68
	v_lshlrev_b32_e32 v186, 16, v69
	v_and_b32_e32 v187, 0xffff0000, v69
	v_lshlrev_b32_e32 v188, 16, v70
	v_and_b32_e32 v189, 0xffff0000, v70
	v_lshlrev_b32_e32 v190, 16, v71
	v_and_b32_e32 v191, 0xffff0000, v71
	v_lshlrev_b32_e32 v192, 16, v72
	v_and_b32_e32 v193, 0xffff0000, v72
	v_lshlrev_b32_e32 v194, 16, v73
	v_and_b32_e32 v195, 0xffff0000, v73
	v_lshlrev_b32_e32 v196, 16, v76
	v_pk_mul_f32 v[200:201], v[184:185], v[184:185]
	v_pk_mul_f32 v[202:203], v[186:187], v[186:187]
	v_add_f32_e32 v198, v200, v201
	v_add_f32_e32 v198, v202, v198
	v_pk_mul_f32 v[200:201], v[188:189], v[188:189]
	v_add_f32_e32 v198, v203, v198
	v_add_f32_e32 v198, v200, v198
	v_pk_mul_f32 v[202:203], v[190:191], v[190:191]
	v_add_f32_e32 v198, v201, v198
	v_add_f32_e32 v198, v202, v198
	v_add_f32_e32 v198, v203, v198
	v_pk_mul_f32 v[200:201], v[192:193], v[192:193]
	v_pk_mul_f32 v[202:203], v[194:195], v[194:195]
	v_add_f32_e32 v199, v200, v201
	v_add_f32_e32 v199, v202, v199
	v_add_f32_e32 v199, v203, v199
	ds_bpermute_b32 v156, v1, v154
	ds_bpermute_b32 v157, v1, v155
	ds_bpermute_b32 v153, v22, v152
	ds_bpermute_b32 v178, v1, v176
	ds_bpermute_b32 v179, v1, v177
	ds_bpermute_b32 v175, v22, v174
	ds_bpermute_b32 v200, v1, v198
	ds_bpermute_b32 v201, v1, v199
	ds_bpermute_b32 v197, v22, v196
	s_waitcnt lgkmcnt(0)
; DI unsigned pk_bf16(float lo, float hi) { f32x2 v = {lo, hi}; hbf16x2 r = __builtin_convertvector(v, hbf16x2); return __builtin_bit_cast(unsigned, r); }
; DI float bflo(unsigned w) { return __uint_as_float(w << 16); }
; DI float bfhi(unsigned w) { return __uint_as_float(w & 0xffff0000u); }
; DI float bf2f(bf16_t b) { return __uint_as_float(((unsigned)b) << 16); }
; DI bf16_t f2bf(float f) { return (bf16_t)(pk_bf16(f, 0.f) & 0xffffu); }
; DI void phase_l0_rows(const Params& p, int G, int bid) {
;     ...
;             ss = wave_sum(ss);
;             const float r = rsqrtf(ss * (1.0f / 512.0f) + EPS);
;             const f32x4 g0 = *(const f32x4*)(p.in[12] + 8 * lane), g1 = *(const f32x4*)(p.in[12] + 8 * lane + 4);
;             u32x4 o; o.x = pk_bf16(v[0] * r * g0[0], v[1] * r * g0[1]); o.y = pk_bf16(v[2] * r * g0[2], v[3] * r * g0[3]);
;             o.z = pk_bf16(v[4] * r * g1[0], v[5] * r * g1[1]); o.w = pk_bf16(v[6] * r * g1[2], v[7] * r * g1[3]);
;             *(u32x4*)(CQN + (size_t)row * 512 + 8 * lane) = o;
;         }
;         {
;             const u32x2 w = *(const u32x2*)(z + 512 + 4 * lane);
;             float v[4] = {bflo(w.x), bfhi(w.x), bflo(w.y), bfhi(w.y)};
;             float ss = v[0] * v[0] + v[1] * v[1] + v[2] * v[2] + v[3] * v[3];
;             ss = wave_sum(ss);
;             const float r = rsqrtf(ss * (1.0f / 256.0f) + EPS);
;             const f32x4 g = *(const f32x4*)(p.in[14] + 4 * lane);
;             u32x2 o; o.x = pk_bf16(v[0] * r * g[0], v[1] * r * g[1]); o.y = pk_bf16(v[2] * r * g[2], v[3] * r * g[3]);
;             *(u32x2*)(CKVN + (size_t)row * 256 + 4 * lane) = o;
;         }
;         {
;             const float x = bf2f(z[768 + lane]);
;             const float xp = __shfl_xor(x, 16);
;             float o = x;
;             if (row >= NCTX) {
;                 const int t = (row - NCTX) & (SEQ - 1), axis = lane >> 5, part = (lane >> 4) & 1, i = lane & 15;
;                 const int pos = axis ? (t & 63) : (t >> 6);
;                 const f32x2 cs = R0[pos * 16 + i];
;                 o = part ? (x * cs[0] + xp * cs[1]) : (x * cs[0] - xp * cs[1]);
;             }
;             KR[(size_t)row * 64 + lane] = f2bf(o);
	v_add_f32_e32 v154, v154, v156
	v_add_f32_e32 v155, v155, v157
	v_add_f32_e32 v176, v176, v178
	v_add_f32_e32 v177, v177, v179
	v_add_f32_e32 v198, v198, v200
	v_add_f32_e32 v199, v199, v201
	ds_bpermute_b32 v156, v22, v154
	ds_bpermute_b32 v157, v22, v155
	ds_bpermute_b32 v178, v22, v176
	ds_bpermute_b32 v179, v22, v177
	ds_bpermute_b32 v200, v22, v198
	ds_bpermute_b32 v201, v22, v199
	s_waitcnt lgkmcnt(0)
	v_add_f32_e32 v154, v154, v156
	v_add_f32_e32 v155, v155, v157
	v_add_f32_e32 v176, v176, v178
	v_add_f32_e32 v177, v177, v179
	v_add_f32_e32 v198, v198, v200
	v_add_f32_e32 v199, v199, v201
	ds_bpermute_b32 v156, v23, v154
	ds_bpermute_b32 v157, v23, v155
	ds_bpermute_b32 v178, v23, v176
	ds_bpermute_b32 v179, v23, v177
	ds_bpermute_b32 v200, v23, v198
	ds_bpermute_b32 v201, v23, v199
	s_waitcnt lgkmcnt(0)
	v_add_f32_e32 v154, v154, v156
	v_add_f32_e32 v155, v155, v157
	v_add_f32_e32 v176, v176, v178
	v_add_f32_e32 v177, v177, v179
	v_add_f32_e32 v198, v198, v200
	v_add_f32_e32 v199, v199, v201
	ds_bpermute_b32 v156, v24, v154
	ds_bpermute_b32 v157, v24, v155
	ds_bpermute_b32 v178, v24, v176
	ds_bpermute_b32 v179, v24, v177
	ds_bpermute_b32 v200, v24, v198
	ds_bpermute_b32 v201, v24, v199
	s_waitcnt lgkmcnt(0)
	v_add_f32_e32 v154, v154, v156
	v_add_f32_e32 v155, v155, v157
	v_add_f32_e32 v176, v176, v178
	v_add_f32_e32 v177, v177, v179
	v_add_f32_e32 v198, v198, v200
	v_add_f32_e32 v199, v199, v201
	ds_bpermute_b32 v156, v25, v154
	ds_bpermute_b32 v157, v25, v155
	ds_bpermute_b32 v178, v25, v176
	ds_bpermute_b32 v179, v25, v177
	ds_bpermute_b32 v200, v25, v198
	ds_bpermute_b32 v201, v25, v199
	s_waitcnt lgkmcnt(0)
	v_add_f32_e32 v154, v154, v156
	v_add_f32_e32 v155, v155, v157
	v_add_f32_e32 v176, v176, v178
	v_add_f32_e32 v177, v177, v179
	v_add_f32_e32 v198, v198, v200
	v_add_f32_e32 v199, v199, v201
	ds_bpermute_b32 v156, v26, v154
	ds_bpermute_b32 v157, v26, v155
	ds_bpermute_b32 v178, v26, v176
	ds_bpermute_b32 v179, v26, v177
	ds_bpermute_b32 v200, v26, v198
	ds_bpermute_b32 v201, v26, v199
	s_waitcnt lgkmcnt(0)
	v_add_f32_e32 v154, v154, v156
	v_add_f32_e32 v155, v155, v157
	v_add_f32_e32 v176, v176, v178
	v_add_f32_e32 v177, v177, v179
	v_add_f32_e32 v198, v198, v200
	v_add_f32_e32 v199, v199, v201
	s_add_i32 s18, s16, 0
	v_fmamk_f32 v154, v154, 0x3b000000, v28
	v_mul_f32_e32 v156, 0x4b800000, v154
	v_cmp_gt_f32_e32 vcc, s14, v154
	s_nop 1
	v_cndmask_b32_e32 v154, v154, v156, vcc
	v_rsq_f32_e32 v158, v154
	s_nop 0
	v_mul_f32_e32 v156, 0x45800000, v158
	s_nop 0
	v_cndmask_b32_e32 v158, v158, v156, vcc
	v_fmamk_f32 v155, v155, 0x3b800000, v28
	v_mul_f32_e32 v156, 0x4b800000, v155
	v_cmp_gt_f32_e32 vcc, s14, v155
	s_nop 1
	v_cndmask_b32_e32 v155, v155, v156, vcc
	v_rsq_f32_e32 v160, v155
	s_nop 0
	v_mul_f32_e32 v156, 0x45800000, v160
	s_nop 0
	v_cndmask_b32_e32 v160, v160, v156, vcc
	v_pk_mul_f32 v[140:141], v[158:159], v[140:141] op_sel_hi:[0,1]
	v_pk_mul_f32 v[142:143], v[158:159], v[142:143] op_sel_hi:[0,1]
	v_pk_mul_f32 v[144:145], v[158:159], v[144:145] op_sel_hi:[0,1]
	v_pk_mul_f32 v[146:147], v[158:159], v[146:147] op_sel_hi:[0,1]
	v_pk_mul_f32 v[140:141], v[34:35], v[140:141]
	v_pk_mul_f32 v[142:143], v[36:37], v[142:143]
	v_pk_mul_f32 v[144:145], v[38:39], v[144:145]
	v_pk_mul_f32 v[146:147], v[40:41], v[146:147]
	s_lshl_b32 s19, s18, 10
	s_add_u32 s19, s19, 0x2b70e000
	s_add_u32 s86, s50, s19
	s_addc_u32 s87, s51, 0
	v_cvt_pk_bf16_f32 v140, v140, v141
	v_cvt_pk_bf16_f32 v141, v142, v143
	v_cvt_pk_bf16_f32 v142, v144, v145
	v_cvt_pk_bf16_f32 v143, v146, v147
	global_store_dwordx4 v2, v[140:143], s[86:87]
	v_pk_mul_f32 v[148:149], v[160:161], v[148:149] op_sel_hi:[0,1]
	v_pk_mul_f32 v[150:151], v[160:161], v[150:151] op_sel_hi:[0,1]
	v_pk_mul_f32 v[148:149], v[42:43], v[148:149]
	v_pk_mul_f32 v[150:151], v[44:45], v[150:151]
	s_lshl_b32 s19, s18, 9
	s_add_u32 s19, s19, 0x2c00e000
	s_add_u32 s88, s50, s19
	s_addc_u32 s89, s51, 0
	v_cvt_pk_bf16_f32 v148, v148, v149
	v_cvt_pk_bf16_f32 v149, v150, v151
	global_store_dwordx2 v16, v[148:149], s[88:89]
	s_cmpk_lt_u32 s18, 0x400
	s_cbranch_scc1 .Ll0r_ns0
	v_mul_f32_e32 v153, v55, v153
	v_cndmask_b32_e64 v153, v153, -v153, s[4:5]
	v_fmac_f32_e32 v153, v54, v152
	v_mov_b32_e32 v152, v153
.Ll0r_ns0:
	s_lshl_b32 s19, s18, 7
	s_add_u32 s19, s19, 0x2c48e000
	s_add_u32 s90, s50, s19
	s_addc_u32 s91, s51, 0
	v_cvt_pk_bf16_f32 v152, v152, v152
	global_store_short v18, v152, s[90:91]
	s_add_i32 s18, s16, 8
	v_fmamk_f32 v176, v176, 0x3b000000, v28
	v_mul_f32_e32 v178, 0x4b800000, v176
	v_cmp_gt_f32_e32 vcc, s14, v176
	s_nop 1
	v_cndmask_b32_e32 v176, v176, v178, vcc
	v_rsq_f32_e32 v180, v176
	s_nop 0
	v_mul_f32_e32 v178, 0x45800000, v180
	s_nop 0
	v_cndmask_b32_e32 v180, v180, v178, vcc
	v_fmamk_f32 v177, v177, 0x3b800000, v28
	v_mul_f32_e32 v178, 0x4b800000, v177
	v_cmp_gt_f32_e32 vcc, s14, v177
	s_nop 1
	v_cndmask_b32_e32 v177, v177, v178, vcc
	v_rsq_f32_e32 v182, v177
	s_nop 0
	v_mul_f32_e32 v178, 0x45800000, v182
	s_nop 0
	v_cndmask_b32_e32 v182, v182, v178, vcc
	v_pk_mul_f32 v[162:163], v[180:181], v[162:163] op_sel_hi:[0,1]
	v_pk_mul_f32 v[164:165], v[180:181], v[164:165] op_sel_hi:[0,1]
	v_pk_mul_f32 v[166:167], v[180:181], v[166:167] op_sel_hi:[0,1]
	v_pk_mul_f32 v[168:169], v[180:181], v[168:169] op_sel_hi:[0,1]
	v_pk_mul_f32 v[162:163], v[34:35], v[162:163]
	v_pk_mul_f32 v[164:165], v[36:37], v[164:165]
	v_pk_mul_f32 v[166:167], v[38:39], v[166:167]
	v_pk_mul_f32 v[168:169], v[40:41], v[168:169]
	s_lshl_b32 s19, s18, 10
	s_add_u32 s19, s19, 0x2b70e000
	s_add_u32 s86, s50, s19
	s_addc_u32 s87, s51, 0
	v_cvt_pk_bf16_f32 v162, v162, v163
	v_cvt_pk_bf16_f32 v163, v164, v165
	v_cvt_pk_bf16_f32 v164, v166, v167
	v_cvt_pk_bf16_f32 v165, v168, v169
	global_store_dwordx4 v2, v[162:165], s[86:87]
	v_pk_mul_f32 v[170:171], v[182:183], v[170:171] op_sel_hi:[0,1]
	v_pk_mul_f32 v[172:173], v[182:183], v[172:173] op_sel_hi:[0,1]
	v_pk_mul_f32 v[170:171], v[42:43], v[170:171]
	v_pk_mul_f32 v[172:173], v[44:45], v[172:173]
	s_lshl_b32 s19, s18, 9
	s_add_u32 s19, s19, 0x2c00e000
	s_add_u32 s88, s50, s19
	s_addc_u32 s89, s51, 0
	v_cvt_pk_bf16_f32 v170, v170, v171
	v_cvt_pk_bf16_f32 v171, v172, v173
	global_store_dwordx2 v16, v[170:171], s[88:89]
	s_cmpk_lt_u32 s18, 0x400
	s_cbranch_scc1 .Ll0r_ns1
	v_mul_f32_e32 v175, v65, v175
	v_cndmask_b32_e64 v175, v175, -v175, s[4:5]
	v_fmac_f32_e32 v175, v64, v174
	v_mov_b32_e32 v174, v175
; DI unsigned pk_bf16(float lo, float hi) { f32x2 v = {lo, hi}; hbf16x2 r = __builtin_convertvector(v, hbf16x2); return __builtin_bit_cast(unsigned, r); }
; DI float bflo(unsigned w) { return __uint_as_float(w << 16); }
; DI float bfhi(unsigned w) { return __uint_as_float(w & 0xffff0000u); }
; DI float bf2f(bf16_t b) { return __uint_as_float(((unsigned)b) << 16); }
; DI bf16_t f2bf(float f) { return (bf16_t)(pk_bf16(f, 0.f) & 0xffffu); }
; DI void phase_l0_rows(const Params& p, int G, int bid) {
;     ...
;             float ss = 0.f;
; #pragma unroll
;             for (int j = 0; j < 8; ++j) ss += v[j] * v[j];
;             ss = wave_sum(ss);
;             const float r = rsqrtf(ss * (1.0f / 512.0f) + EPS);
;             const f32x4 g0 = *(const f32x4*)(p.in[12] + 8 * lane), g1 = *(const f32x4*)(p.in[12] + 8 * lane + 4);
;             u32x4 o; o.x = pk_bf16(v[0] * r * g0[0], v[1] * r * g0[1]); o.y = pk_bf16(v[2] * r * g0[2], v[3] * r * g0[3]);
;             o.z = pk_bf16(v[4] * r * g1[0], v[5] * r * g1[1]); o.w = pk_bf16(v[6] * r * g1[2], v[7] * r * g1[3]);
;             *(u32x4*)(CQN + (size_t)row * 512 + 8 * lane) = o;
;         }
;         {
;             const u32x2 w = *(const u32x2*)(z + 512 + 4 * lane);
;             float v[4] = {bflo(w.x), bfhi(w.x), bflo(w.y), bfhi(w.y)};
;             float ss = v[0] * v[0] + v[1] * v[1] + v[2] * v[2] + v[3] * v[3];
;             ss = wave_sum(ss);
;             const float r = rsqrtf(ss * (1.0f / 256.0f) + EPS);
;             const f32x4 g = *(const f32x4*)(p.in[14] + 4 * lane);
;             u32x2 o; o.x = pk_bf16(v[0] * r * g[0], v[1] * r * g[1]); o.y = pk_bf16(v[2] * r * g[2], v[3] * r * g[3]);
;             *(u32x2*)(CKVN + (size_t)row * 256 + 4 * lane) = o;
;         }
;         {
;             const float x = bf2f(z[768 + lane]);
;             const float xp = __shfl_xor(x, 16);
;             float o = x;
;             if (row >= NCTX) {
;                 const int t = (row - NCTX) & (SEQ - 1), axis = lane >> 5, part = (lane >> 4) & 1, i = lane & 15;
;                 const int pos = axis ? (t & 63) : (t >> 6);
;                 const f32x2 cs = R0[pos * 16 + i];
;                 o = part ? (x * cs[0] + xp * cs[1]) : (x * cs[0] - xp * cs[1]);
;             }
;             KR[(size_t)row * 64 + lane] = f2bf(o);
.Ll0r_ns1:
	s_lshl_b32 s19, s18, 7
	s_add_u32 s19, s19, 0x2c48e000
	s_add_u32 s90, s50, s19
	s_addc_u32 s91, s51, 0
	v_cvt_pk_bf16_f32 v174, v174, v174
	global_store_short v18, v174, s[90:91]
	s_add_i32 s18, s16, 16
	v_fmamk_f32 v198, v198, 0x3b000000, v28
	v_mul_f32_e32 v200, 0x4b800000, v198
	v_cmp_gt_f32_e32 vcc, s14, v198
	s_nop 1
	v_cndmask_b32_e32 v198, v198, v200, vcc
	v_rsq_f32_e32 v202, v198
	s_nop 0
	v_mul_f32_e32 v200, 0x45800000, v202
	s_nop 0
	v_cndmask_b32_e32 v202, v202, v200, vcc
	v_fmamk_f32 v199, v199, 0x3b800000, v28
	v_mul_f32_e32 v200, 0x4b800000, v199
	v_cmp_gt_f32_e32 vcc, s14, v199
	s_nop 1
	v_cndmask_b32_e32 v199, v199, v200, vcc
	v_rsq_f32_e32 v204, v199
	s_nop 0
	v_mul_f32_e32 v200, 0x45800000, v204
	s_nop 0
	v_cndmask_b32_e32 v204, v204, v200, vcc
	v_pk_mul_f32 v[184:185], v[202:203], v[184:185] op_sel_hi:[0,1]
	v_pk_mul_f32 v[186:187], v[202:203], v[186:187] op_sel_hi:[0,1]
	v_pk_mul_f32 v[188:189], v[202:203], v[188:189] op_sel_hi:[0,1]
	v_pk_mul_f32 v[190:191], v[202:203], v[190:191] op_sel_hi:[0,1]
	v_pk_mul_f32 v[184:185], v[34:35], v[184:185]
	v_pk_mul_f32 v[186:187], v[36:37], v[186:187]
	v_pk_mul_f32 v[188:189], v[38:39], v[188:189]
	v_pk_mul_f32 v[190:191], v[40:41], v[190:191]
	s_lshl_b32 s19, s18, 10
	s_add_u32 s19, s19, 0x2b70e000
	s_add_u32 s86, s50, s19
	s_addc_u32 s87, s51, 0
	v_cvt_pk_bf16_f32 v184, v184, v185
	v_cvt_pk_bf16_f32 v185, v186, v187
	v_cvt_pk_bf16_f32 v186, v188, v189
	v_cvt_pk_bf16_f32 v187, v190, v191
	global_store_dwordx4 v2, v[184:187], s[86:87]
	v_pk_mul_f32 v[192:193], v[204:205], v[192:193] op_sel_hi:[0,1]
	v_pk_mul_f32 v[194:195], v[204:205], v[194:195] op_sel_hi:[0,1]
	v_pk_mul_f32 v[192:193], v[42:43], v[192:193]
	v_pk_mul_f32 v[194:195], v[44:45], v[194:195]
	s_lshl_b32 s19, s18, 9
	s_add_u32 s19, s19, 0x2c00e000
	s_add_u32 s88, s50, s19
	s_addc_u32 s89, s51, 0
	v_cvt_pk_bf16_f32 v192, v192, v193
	v_cvt_pk_bf16_f32 v193, v194, v195
	global_store_dwordx2 v16, v[192:193], s[88:89]
	s_cmpk_lt_u32 s18, 0x400
	s_cbranch_scc1 .Ll0r_ns2
	v_mul_f32_e32 v197, v75, v197
	v_cndmask_b32_e64 v197, v197, -v197, s[4:5]
	v_fmac_f32_e32 v197, v74, v196
	v_mov_b32_e32 v196, v197
.Ll0r_ns2:
	s_lshl_b32 s19, s18, 7
	s_add_u32 s19, s19, 0x2c48e000
	s_add_u32 s90, s50, s19
	s_addc_u32 s91, s51, 0
	v_cvt_pk_bf16_f32 v196, v196, v196
	global_store_short v18, v196, s[90:91]
	v_lshlrev_b32_e32 v140, 16, v78
	v_and_b32_e32 v141, 0xffff0000, v78
	v_lshlrev_b32_e32 v142, 16, v79
	v_and_b32_e32 v143, 0xffff0000, v79
	v_lshlrev_b32_e32 v144, 16, v80
	v_and_b32_e32 v145, 0xffff0000, v80
	v_lshlrev_b32_e32 v146, 16, v81
	v_and_b32_e32 v147, 0xffff0000, v81
	v_lshlrev_b32_e32 v148, 16, v82
	v_and_b32_e32 v149, 0xffff0000, v82
	v_lshlrev_b32_e32 v150, 16, v83
	v_and_b32_e32 v151, 0xffff0000, v83
	v_lshlrev_b32_e32 v152, 16, v86
	v_pk_mul_f32 v[156:157], v[140:141], v[140:141]
	v_pk_mul_f32 v[158:159], v[142:143], v[142:143]
	v_add_f32_e32 v154, v156, v157
	v_add_f32_e32 v154, v158, v154
	v_pk_mul_f32 v[156:157], v[144:145], v[144:145]
	v_add_f32_e32 v154, v159, v154
	v_add_f32_e32 v154, v156, v154
	v_pk_mul_f32 v[158:159], v[146:147], v[146:147]
	v_add_f32_e32 v154, v157, v154
	v_add_f32_e32 v154, v158, v154
	v_add_f32_e32 v154, v159, v154
	v_pk_mul_f32 v[156:157], v[148:149], v[148:149]
	v_pk_mul_f32 v[158:159], v[150:151], v[150:151]
	v_add_f32_e32 v155, v156, v157
	v_add_f32_e32 v155, v158, v155
	v_add_f32_e32 v155, v159, v155
	v_lshlrev_b32_e32 v162, 16, v88
	v_and_b32_e32 v163, 0xffff0000, v88
	v_lshlrev_b32_e32 v164, 16, v89
	v_and_b32_e32 v165, 0xffff0000, v89
	v_lshlrev_b32_e32 v166, 16, v90
	v_and_b32_e32 v167, 0xffff0000, v90
	v_lshlrev_b32_e32 v168, 16, v91
	v_and_b32_e32 v169, 0xffff0000, v91
	v_lshlrev_b32_e32 v170, 16, v92
	v_and_b32_e32 v171, 0xffff0000, v92
	v_lshlrev_b32_e32 v172, 16, v93
	v_and_b32_e32 v173, 0xffff0000, v93
	v_lshlrev_b32_e32 v174, 16, v96
	v_pk_mul_f32 v[178:179], v[162:163], v[162:163]
	v_pk_mul_f32 v[180:181], v[164:165], v[164:165]
	v_add_f32_e32 v176, v178, v179
	v_add_f32_e32 v176, v180, v176
	v_pk_mul_f32 v[178:179], v[166:167], v[166:167]
	v_add_f32_e32 v176, v181, v176
	v_add_f32_e32 v176, v178, v176
	v_pk_mul_f32 v[180:181], v[168:169], v[168:169]
	v_add_f32_e32 v176, v179, v176
	v_add_f32_e32 v176, v180, v176
	v_add_f32_e32 v176, v181, v176
	v_pk_mul_f32 v[178:179], v[170:171], v[170:171]
	v_pk_mul_f32 v[180:181], v[172:173], v[172:173]
	v_add_f32_e32 v177, v178, v179
	v_add_f32_e32 v177, v180, v177
	v_add_f32_e32 v177, v181, v177
	v_lshlrev_b32_e32 v184, 16, v98
	v_and_b32_e32 v185, 0xffff0000, v98
	v_lshlrev_b32_e32 v186, 16, v99
	v_and_b32_e32 v187, 0xffff0000, v99
	v_lshlrev_b32_e32 v188, 16, v100
	v_and_b32_e32 v189, 0xffff0000, v100
	v_lshlrev_b32_e32 v190, 16, v101
	v_and_b32_e32 v191, 0xffff0000, v101
	v_lshlrev_b32_e32 v192, 16, v102
	v_and_b32_e32 v193, 0xffff0000, v102
	v_lshlrev_b32_e32 v194, 16, v103
	v_and_b32_e32 v195, 0xffff0000, v103
	v_lshlrev_b32_e32 v196, 16, v106
	v_pk_mul_f32 v[200:201], v[184:185], v[184:185]
	v_pk_mul_f32 v[202:203], v[186:187], v[186:187]
	v_add_f32_e32 v198, v200, v201
	v_add_f32_e32 v198, v202, v198
	v_pk_mul_f32 v[200:201], v[188:189], v[188:189]
	v_add_f32_e32 v198, v203, v198
	v_add_f32_e32 v198, v200, v198
	v_pk_mul_f32 v[202:203], v[190:191], v[190:191]
	v_add_f32_e32 v198, v201, v198
	v_add_f32_e32 v198, v202, v198
	v_add_f32_e32 v198, v203, v198
	v_pk_mul_f32 v[200:201], v[192:193], v[192:193]
	v_pk_mul_f32 v[202:203], v[194:195], v[194:195]
	v_add_f32_e32 v199, v200, v201
	v_add_f32_e32 v199, v202, v199
	v_add_f32_e32 v199, v203, v199
	ds_bpermute_b32 v156, v1, v154
	ds_bpermute_b32 v157, v1, v155
	ds_bpermute_b32 v153, v22, v152
	ds_bpermute_b32 v178, v1, v176
	ds_bpermute_b32 v179, v1, v177
	ds_bpermute_b32 v175, v22, v174
	ds_bpermute_b32 v200, v1, v198
	ds_bpermute_b32 v201, v1, v199
	ds_bpermute_b32 v197, v22, v196
	s_waitcnt lgkmcnt(0)
; DI unsigned pk_bf16(float lo, float hi) { f32x2 v = {lo, hi}; hbf16x2 r = __builtin_convertvector(v, hbf16x2); return __builtin_bit_cast(unsigned, r); }
; DI float bflo(unsigned w) { return __uint_as_float(w << 16); }
; DI float bfhi(unsigned w) { return __uint_as_float(w & 0xffff0000u); }
; DI float bf2f(bf16_t b) { return __uint_as_float(((unsigned)b) << 16); }
; DI bf16_t f2bf(float f) { return (bf16_t)(pk_bf16(f, 0.f) & 0xffffu); }
; DI void phase_l0_rows(const Params& p, int G, int bid) {
;     ...
;             ss = wave_sum(ss);
;             const float r = rsqrtf(ss * (1.0f / 512.0f) + EPS);
;             const f32x4 g0 = *(const f32x4*)(p.in[12] + 8 * lane), g1 = *(const f32x4*)(p.in[12] + 8 * lane + 4);
;             u32x4 o; o.x = pk_bf16(v[0] * r * g0[0], v[1] * r * g0[1]); o.y = pk_bf16(v[2] * r * g0[2], v[3] * r * g0[3]);
;             o.z = pk_bf16(v[4] * r * g1[0], v[5] * r * g1[1]); o.w = pk_bf16(v[6] * r * g1[2], v[7] * r * g1[3]);
;             *(u32x4*)(CQN + (size_t)row * 512 + 8 * lane) = o;
;         }
;         {
;             const u32x2 w = *(const u32x2*)(z + 512 + 4 * lane);
;             float v[4] = {bflo(w.x), bfhi(w.x), bflo(w.y), bfhi(w.y)};
;             float ss = v[0] * v[0] + v[1] * v[1] + v[2] * v[2] + v[3] * v[3];
;             ss = wave_sum(ss);
;             const float r = rsqrtf(ss * (1.0f / 256.0f) + EPS);
;             const f32x4 g = *(const f32x4*)(p.in[14] + 4 * lane);
;             u32x2 o; o.x = pk_bf16(v[0] * r * g[0], v[1] * r * g[1]); o.y = pk_bf16(v[2] * r * g[2], v[3] * r * g[3]);
;             *(u32x2*)(CKVN + (size_t)row * 256 + 4 * lane) = o;
;         }
;         {
;             const float x = bf2f(z[768 + lane]);
;             const float xp = __shfl_xor(x, 16);
;             float o = x;
;             if (row >= NCTX) {
;                 const int t = (row - NCTX) & (SEQ - 1), axis = lane >> 5, part = (lane >> 4) & 1, i = lane & 15;
;                 const int pos = axis ? (t & 63) : (t >> 6);
;                 const f32x2 cs = R0[pos * 16 + i];
;                 o = part ? (x * cs[0] + xp * cs[1]) : (x * cs[0] - xp * cs[1]);
;             }
;             KR[(size_t)row * 64 + lane] = f2bf(o);
	v_add_f32_e32 v154, v154, v156
	v_add_f32_e32 v155, v155, v157
	v_add_f32_e32 v176, v176, v178
	v_add_f32_e32 v177, v177, v179
	v_add_f32_e32 v198, v198, v200
	v_add_f32_e32 v199, v199, v201
	ds_bpermute_b32 v156, v22, v154
	ds_bpermute_b32 v157, v22, v155
	ds_bpermute_b32 v178, v22, v176
	ds_bpermute_b32 v179, v22, v177
	ds_bpermute_b32 v200, v22, v198
	ds_bpermute_b32 v201, v22, v199
	s_waitcnt lgkmcnt(0)
	v_add_f32_e32 v154, v154, v156
	v_add_f32_e32 v155, v155, v157
	v_add_f32_e32 v176, v176, v178
	v_add_f32_e32 v177, v177, v179
	v_add_f32_e32 v198, v198, v200
	v_add_f32_e32 v199, v199, v201
	ds_bpermute_b32 v156, v23, v154
	ds_bpermute_b32 v157, v23, v155
	ds_bpermute_b32 v178, v23, v176
	ds_bpermute_b32 v179, v23, v177
	ds_bpermute_b32 v200, v23, v198
	ds_bpermute_b32 v201, v23, v199
	s_waitcnt lgkmcnt(0)
	v_add_f32_e32 v154, v154, v156
	v_add_f32_e32 v155, v155, v157
	v_add_f32_e32 v176, v176, v178
	v_add_f32_e32 v177, v177, v179
	v_add_f32_e32 v198, v198, v200
	v_add_f32_e32 v199, v199, v201
	ds_bpermute_b32 v156, v24, v154
	ds_bpermute_b32 v157, v24, v155
	ds_bpermute_b32 v178, v24, v176
	ds_bpermute_b32 v179, v24, v177
	ds_bpermute_b32 v200, v24, v198
	ds_bpermute_b32 v201, v24, v199
	s_waitcnt lgkmcnt(0)
	v_add_f32_e32 v154, v154, v156
	v_add_f32_e32 v155, v155, v157
	v_add_f32_e32 v176, v176, v178
	v_add_f32_e32 v177, v177, v179
	v_add_f32_e32 v198, v198, v200
	v_add_f32_e32 v199, v199, v201
	ds_bpermute_b32 v156, v25, v154
	ds_bpermute_b32 v157, v25, v155
	ds_bpermute_b32 v178, v25, v176
	ds_bpermute_b32 v179, v25, v177
	ds_bpermute_b32 v200, v25, v198
	ds_bpermute_b32 v201, v25, v199
	s_waitcnt lgkmcnt(0)
	v_add_f32_e32 v154, v154, v156
	v_add_f32_e32 v155, v155, v157
	v_add_f32_e32 v176, v176, v178
	v_add_f32_e32 v177, v177, v179
	v_add_f32_e32 v198, v198, v200
	v_add_f32_e32 v199, v199, v201
	ds_bpermute_b32 v156, v26, v154
	ds_bpermute_b32 v157, v26, v155
	ds_bpermute_b32 v178, v26, v176
	ds_bpermute_b32 v179, v26, v177
	ds_bpermute_b32 v200, v26, v198
	ds_bpermute_b32 v201, v26, v199
	s_waitcnt lgkmcnt(0)
	v_add_f32_e32 v154, v154, v156
	v_add_f32_e32 v155, v155, v157
	v_add_f32_e32 v176, v176, v178
	v_add_f32_e32 v177, v177, v179
	v_add_f32_e32 v198, v198, v200
	v_add_f32_e32 v199, v199, v201
	s_add_i32 s18, s16, 24
	v_fmamk_f32 v154, v154, 0x3b000000, v28
	v_mul_f32_e32 v156, 0x4b800000, v154
	v_cmp_gt_f32_e32 vcc, s14, v154
	s_nop 1
	v_cndmask_b32_e32 v154, v154, v156, vcc
	v_rsq_f32_e32 v158, v154
	s_nop 0
	v_mul_f32_e32 v156, 0x45800000, v158
	s_nop 0
	v_cndmask_b32_e32 v158, v158, v156, vcc
	v_fmamk_f32 v155, v155, 0x3b800000, v28
	v_mul_f32_e32 v156, 0x4b800000, v155
	v_cmp_gt_f32_e32 vcc, s14, v155
	s_nop 1
	v_cndmask_b32_e32 v155, v155, v156, vcc
	v_rsq_f32_e32 v160, v155
	s_nop 0
	v_mul_f32_e32 v156, 0x45800000, v160
	s_nop 0
	v_cndmask_b32_e32 v160, v160, v156, vcc
	v_pk_mul_f32 v[140:141], v[158:159], v[140:141] op_sel_hi:[0,1]
	v_pk_mul_f32 v[142:143], v[158:159], v[142:143] op_sel_hi:[0,1]
	v_pk_mul_f32 v[144:145], v[158:159], v[144:145] op_sel_hi:[0,1]
	v_pk_mul_f32 v[146:147], v[158:159], v[146:147] op_sel_hi:[0,1]
	v_pk_mul_f32 v[140:141], v[34:35], v[140:141]
	v_pk_mul_f32 v[142:143], v[36:37], v[142:143]
	v_pk_mul_f32 v[144:145], v[38:39], v[144:145]
	v_pk_mul_f32 v[146:147], v[40:41], v[146:147]
	s_lshl_b32 s19, s18, 10
	s_add_u32 s19, s19, 0x2b70e000
	s_add_u32 s86, s50, s19
	s_addc_u32 s87, s51, 0
	v_cvt_pk_bf16_f32 v140, v140, v141
	v_cvt_pk_bf16_f32 v141, v142, v143
	v_cvt_pk_bf16_f32 v142, v144, v145
	v_cvt_pk_bf16_f32 v143, v146, v147
	global_store_dwordx4 v2, v[140:143], s[86:87]
	v_pk_mul_f32 v[148:149], v[160:161], v[148:149] op_sel_hi:[0,1]
	v_pk_mul_f32 v[150:151], v[160:161], v[150:151] op_sel_hi:[0,1]
	v_pk_mul_f32 v[148:149], v[42:43], v[148:149]
	v_pk_mul_f32 v[150:151], v[44:45], v[150:151]
	s_lshl_b32 s19, s18, 9
	s_add_u32 s19, s19, 0x2c00e000
	s_add_u32 s88, s50, s19
	s_addc_u32 s89, s51, 0
	v_cvt_pk_bf16_f32 v148, v148, v149
	v_cvt_pk_bf16_f32 v149, v150, v151
	global_store_dwordx2 v16, v[148:149], s[88:89]
	s_cmpk_lt_u32 s18, 0x400
	s_cbranch_scc1 .Ll0r_ns3
	v_mul_f32_e32 v153, v85, v153
	v_cndmask_b32_e64 v153, v153, -v153, s[4:5]
	v_fmac_f32_e32 v153, v84, v152
	v_mov_b32_e32 v152, v153
.Ll0r_ns3:
	s_lshl_b32 s19, s18, 7
	s_add_u32 s19, s19, 0x2c48e000
	s_add_u32 s90, s50, s19
	s_addc_u32 s91, s51, 0
	v_cvt_pk_bf16_f32 v152, v152, v152
	global_store_short v18, v152, s[90:91]
	s_add_i32 s18, s16, 32
	v_fmamk_f32 v176, v176, 0x3b000000, v28
	v_mul_f32_e32 v178, 0x4b800000, v176
	v_cmp_gt_f32_e32 vcc, s14, v176
	s_nop 1
	v_cndmask_b32_e32 v176, v176, v178, vcc
	v_rsq_f32_e32 v180, v176
	s_nop 0
	v_mul_f32_e32 v178, 0x45800000, v180
	s_nop 0
	v_cndmask_b32_e32 v180, v180, v178, vcc
	v_fmamk_f32 v177, v177, 0x3b800000, v28
	v_mul_f32_e32 v178, 0x4b800000, v177
	v_cmp_gt_f32_e32 vcc, s14, v177
	s_nop 1
	v_cndmask_b32_e32 v177, v177, v178, vcc
	v_rsq_f32_e32 v182, v177
	s_nop 0
	v_mul_f32_e32 v178, 0x45800000, v182
	s_nop 0
	v_cndmask_b32_e32 v182, v182, v178, vcc
	v_pk_mul_f32 v[162:163], v[180:181], v[162:163] op_sel_hi:[0,1]
	v_pk_mul_f32 v[164:165], v[180:181], v[164:165] op_sel_hi:[0,1]
	v_pk_mul_f32 v[166:167], v[180:181], v[166:167] op_sel_hi:[0,1]
	v_pk_mul_f32 v[168:169], v[180:181], v[168:169] op_sel_hi:[0,1]
	v_pk_mul_f32 v[162:163], v[34:35], v[162:163]
	v_pk_mul_f32 v[164:165], v[36:37], v[164:165]
	v_pk_mul_f32 v[166:167], v[38:39], v[166:167]
	v_pk_mul_f32 v[168:169], v[40:41], v[168:169]
	s_lshl_b32 s19, s18, 10
	s_add_u32 s19, s19, 0x2b70e000
	s_add_u32 s86, s50, s19
	s_addc_u32 s87, s51, 0
	v_cvt_pk_bf16_f32 v162, v162, v163
	v_cvt_pk_bf16_f32 v163, v164, v165
	v_cvt_pk_bf16_f32 v164, v166, v167
	v_cvt_pk_bf16_f32 v165, v168, v169
	global_store_dwordx4 v2, v[162:165], s[86:87]
	v_pk_mul_f32 v[170:171], v[182:183], v[170:171] op_sel_hi:[0,1]
	v_pk_mul_f32 v[172:173], v[182:183], v[172:173] op_sel_hi:[0,1]
	v_pk_mul_f32 v[170:171], v[42:43], v[170:171]
	v_pk_mul_f32 v[172:173], v[44:45], v[172:173]
	s_lshl_b32 s19, s18, 9
	s_add_u32 s19, s19, 0x2c00e000
	s_add_u32 s88, s50, s19
	s_addc_u32 s89, s51, 0
	v_cvt_pk_bf16_f32 v170, v170, v171
	v_cvt_pk_bf16_f32 v171, v172, v173
	global_store_dwordx2 v16, v[170:171], s[88:89]
	s_cmpk_lt_u32 s18, 0x400
	s_cbranch_scc1 .Ll0r_ns4
	v_mul_f32_e32 v175, v95, v175
	v_cndmask_b32_e64 v175, v175, -v175, s[4:5]
	v_fmac_f32_e32 v175, v94, v174
	v_mov_b32_e32 v174, v175
; DI unsigned pk_bf16(float lo, float hi) { f32x2 v = {lo, hi}; hbf16x2 r = __builtin_convertvector(v, hbf16x2); return __builtin_bit_cast(unsigned, r); }
; DI float bflo(unsigned w) { return __uint_as_float(w << 16); }
; DI float bfhi(unsigned w) { return __uint_as_float(w & 0xffff0000u); }
; DI float bf2f(bf16_t b) { return __uint_as_float(((unsigned)b) << 16); }
; DI bf16_t f2bf(float f) { return (bf16_t)(pk_bf16(f, 0.f) & 0xffffu); }
; DI void phase_l0_rows(const Params& p, int G, int bid) {
;     ...
;             float ss = 0.f;
; #pragma unroll
;             for (int j = 0; j < 8; ++j) ss += v[j] * v[j];
;             ss = wave_sum(ss);
;             const float r = rsqrtf(ss * (1.0f / 512.0f) + EPS);
;             const f32x4 g0 = *(const f32x4*)(p.in[12] + 8 * lane), g1 = *(const f32x4*)(p.in[12] + 8 * lane + 4);
;             u32x4 o; o.x = pk_bf16(v[0] * r * g0[0], v[1] * r * g0[1]); o.y = pk_bf16(v[2] * r * g0[2], v[3] * r * g0[3]);
;             o.z = pk_bf16(v[4] * r * g1[0], v[5] * r * g1[1]); o.w = pk_bf16(v[6] * r * g1[2], v[7] * r * g1[3]);
;             *(u32x4*)(CQN + (size_t)row * 512 + 8 * lane) = o;
;         }
;         {
;             const u32x2 w = *(const u32x2*)(z + 512 + 4 * lane);
;             float v[4] = {bflo(w.x), bfhi(w.x), bflo(w.y), bfhi(w.y)};
;             float ss = v[0] * v[0] + v[1] * v[1] + v[2] * v[2] + v[3] * v[3];
;             ss = wave_sum(ss);
;             const float r = rsqrtf(ss * (1.0f / 256.0f) + EPS);
;             const f32x4 g = *(const f32x4*)(p.in[14] + 4 * lane);
;             u32x2 o; o.x = pk_bf16(v[0] * r * g[0], v[1] * r * g[1]); o.y = pk_bf16(v[2] * r * g[2], v[3] * r * g[3]);
;             *(u32x2*)(CKVN + (size_t)row * 256 + 4 * lane) = o;
;         }
;         {
;             const float x = bf2f(z[768 + lane]);
;             const float xp = __shfl_xor(x, 16);
;             float o = x;
;             if (row >= NCTX) {
;                 const int t = (row - NCTX) & (SEQ - 1), axis = lane >> 5, part = (lane >> 4) & 1, i = lane & 15;
;                 const int pos = axis ? (t & 63) : (t >> 6);
;                 const f32x2 cs = R0[pos * 16 + i];
;                 o = part ? (x * cs[0] + xp * cs[1]) : (x * cs[0] - xp * cs[1]);
;             }
;             KR[(size_t)row * 64 + lane] = f2bf(o);
.Ll0r_ns4:
	s_lshl_b32 s19, s18, 7
	s_add_u32 s19, s19, 0x2c48e000
	s_add_u32 s90, s50, s19
	s_addc_u32 s91, s51, 0
	v_cvt_pk_bf16_f32 v174, v174, v174
	global_store_short v18, v174, s[90:91]
	s_add_i32 s18, s16, 40
	v_fmamk_f32 v198, v198, 0x3b000000, v28
	v_mul_f32_e32 v200, 0x4b800000, v198
	v_cmp_gt_f32_e32 vcc, s14, v198
	s_nop 1
	v_cndmask_b32_e32 v198, v198, v200, vcc
	v_rsq_f32_e32 v202, v198
	s_nop 0
	v_mul_f32_e32 v200, 0x45800000, v202
	s_nop 0
	v_cndmask_b32_e32 v202, v202, v200, vcc
	v_fmamk_f32 v199, v199, 0x3b800000, v28
	v_mul_f32_e32 v200, 0x4b800000, v199
	v_cmp_gt_f32_e32 vcc, s14, v199
	s_nop 1
	v_cndmask_b32_e32 v199, v199, v200, vcc
	v_rsq_f32_e32 v204, v199
	s_nop 0
	v_mul_f32_e32 v200, 0x45800000, v204
	s_nop 0
	v_cndmask_b32_e32 v204, v204, v200, vcc
	v_pk_mul_f32 v[184:185], v[202:203], v[184:185] op_sel_hi:[0,1]
	v_pk_mul_f32 v[186:187], v[202:203], v[186:187] op_sel_hi:[0,1]
	v_pk_mul_f32 v[188:189], v[202:203], v[188:189] op_sel_hi:[0,1]
	v_pk_mul_f32 v[190:191], v[202:203], v[190:191] op_sel_hi:[0,1]
	v_pk_mul_f32 v[184:185], v[34:35], v[184:185]
	v_pk_mul_f32 v[186:187], v[36:37], v[186:187]
	v_pk_mul_f32 v[188:189], v[38:39], v[188:189]
	v_pk_mul_f32 v[190:191], v[40:41], v[190:191]
	s_lshl_b32 s19, s18, 10
	s_add_u32 s19, s19, 0x2b70e000
	s_add_u32 s86, s50, s19
	s_addc_u32 s87, s51, 0
	v_cvt_pk_bf16_f32 v184, v184, v185
	v_cvt_pk_bf16_f32 v185, v186, v187
	v_cvt_pk_bf16_f32 v186, v188, v189
	v_cvt_pk_bf16_f32 v187, v190, v191
	global_store_dwordx4 v2, v[184:187], s[86:87]
	v_pk_mul_f32 v[192:193], v[204:205], v[192:193] op_sel_hi:[0,1]
	v_pk_mul_f32 v[194:195], v[204:205], v[194:195] op_sel_hi:[0,1]
	v_pk_mul_f32 v[192:193], v[42:43], v[192:193]
	v_pk_mul_f32 v[194:195], v[44:45], v[194:195]
	s_lshl_b32 s19, s18, 9
	s_add_u32 s19, s19, 0x2c00e000
	s_add_u32 s88, s50, s19
	s_addc_u32 s89, s51, 0
	v_cvt_pk_bf16_f32 v192, v192, v193
	v_cvt_pk_bf16_f32 v193, v194, v195
	global_store_dwordx2 v16, v[192:193], s[88:89]
	s_cmpk_lt_u32 s18, 0x400
	s_cbranch_scc1 .Ll0r_ns5
	v_mul_f32_e32 v197, v105, v197
	v_cndmask_b32_e64 v197, v197, -v197, s[4:5]
	v_fmac_f32_e32 v197, v104, v196
	v_mov_b32_e32 v196, v197
.Ll0r_ns5:
	s_lshl_b32 s19, s18, 7
	s_add_u32 s19, s19, 0x2c48e000
	s_add_u32 s90, s50, s19
	s_addc_u32 s91, s51, 0
	v_cvt_pk_bf16_f32 v196, v196, v196
	global_store_short v18, v196, s[90:91]
	v_lshlrev_b32_e32 v140, 16, v108
	v_and_b32_e32 v141, 0xffff0000, v108
	v_lshlrev_b32_e32 v142, 16, v109
	v_and_b32_e32 v143, 0xffff0000, v109
	v_lshlrev_b32_e32 v144, 16, v110
	v_and_b32_e32 v145, 0xffff0000, v110
	v_lshlrev_b32_e32 v146, 16, v111
	v_and_b32_e32 v147, 0xffff0000, v111
	v_lshlrev_b32_e32 v148, 16, v112
	v_and_b32_e32 v149, 0xffff0000, v112
	v_lshlrev_b32_e32 v150, 16, v113
	v_and_b32_e32 v151, 0xffff0000, v113
	v_lshlrev_b32_e32 v152, 16, v116
	v_pk_mul_f32 v[156:157], v[140:141], v[140:141]
	v_pk_mul_f32 v[158:159], v[142:143], v[142:143]
	v_add_f32_e32 v154, v156, v157
	v_add_f32_e32 v154, v158, v154
	v_pk_mul_f32 v[156:157], v[144:145], v[144:145]
	v_add_f32_e32 v154, v159, v154
	v_add_f32_e32 v154, v156, v154
	v_pk_mul_f32 v[158:159], v[146:147], v[146:147]
	v_add_f32_e32 v154, v157, v154
	v_add_f32_e32 v154, v158, v154
	v_add_f32_e32 v154, v159, v154
	v_pk_mul_f32 v[156:157], v[148:149], v[148:149]
	v_pk_mul_f32 v[158:159], v[150:151], v[150:151]
	v_add_f32_e32 v155, v156, v157
	v_add_f32_e32 v155, v158, v155
	v_add_f32_e32 v155, v159, v155
	v_lshlrev_b32_e32 v162, 16, v118
	v_and_b32_e32 v163, 0xffff0000, v118
	v_lshlrev_b32_e32 v164, 16, v119
	v_and_b32_e32 v165, 0xffff0000, v119
	v_lshlrev_b32_e32 v166, 16, v120
	v_and_b32_e32 v167, 0xffff0000, v120
	v_lshlrev_b32_e32 v168, 16, v121
	v_and_b32_e32 v169, 0xffff0000, v121
	v_lshlrev_b32_e32 v170, 16, v122
	v_and_b32_e32 v171, 0xffff0000, v122
	v_lshlrev_b32_e32 v172, 16, v123
	v_and_b32_e32 v173, 0xffff0000, v123
	v_lshlrev_b32_e32 v174, 16, v126
	v_pk_mul_f32 v[178:179], v[162:163], v[162:163]
	v_pk_mul_f32 v[180:181], v[164:165], v[164:165]
	v_add_f32_e32 v176, v178, v179
	v_add_f32_e32 v176, v180, v176
	v_pk_mul_f32 v[178:179], v[166:167], v[166:167]
	v_add_f32_e32 v176, v181, v176
	v_add_f32_e32 v176, v178, v176
	v_pk_mul_f32 v[180:181], v[168:169], v[168:169]
	v_add_f32_e32 v176, v179, v176
	v_add_f32_e32 v176, v180, v176
	v_add_f32_e32 v176, v181, v176
	v_pk_mul_f32 v[178:179], v[170:171], v[170:171]
	v_pk_mul_f32 v[180:181], v[172:173], v[172:173]
	v_add_f32_e32 v177, v178, v179
	v_add_f32_e32 v177, v180, v177
	v_add_f32_e32 v177, v181, v177
	v_lshlrev_b32_e32 v184, 16, v128
	v_and_b32_e32 v185, 0xffff0000, v128
	v_lshlrev_b32_e32 v186, 16, v129
	v_and_b32_e32 v187, 0xffff0000, v129
	v_lshlrev_b32_e32 v188, 16, v130
	v_and_b32_e32 v189, 0xffff0000, v130
	v_lshlrev_b32_e32 v190, 16, v131
	v_and_b32_e32 v191, 0xffff0000, v131
	v_lshlrev_b32_e32 v192, 16, v132
	v_and_b32_e32 v193, 0xffff0000, v132
	v_lshlrev_b32_e32 v194, 16, v133
	v_and_b32_e32 v195, 0xffff0000, v133
	v_lshlrev_b32_e32 v196, 16, v136
	v_pk_mul_f32 v[200:201], v[184:185], v[184:185]
	v_pk_mul_f32 v[202:203], v[186:187], v[186:187]
	v_add_f32_e32 v198, v200, v201
	v_add_f32_e32 v198, v202, v198
	v_pk_mul_f32 v[200:201], v[188:189], v[188:189]
	v_add_f32_e32 v198, v203, v198
	v_add_f32_e32 v198, v200, v198
	v_pk_mul_f32 v[202:203], v[190:191], v[190:191]
	v_add_f32_e32 v198, v201, v198
	v_add_f32_e32 v198, v202, v198
	v_add_f32_e32 v198, v203, v198
	v_pk_mul_f32 v[200:201], v[192:193], v[192:193]
	v_pk_mul_f32 v[202:203], v[194:195], v[194:195]
	v_add_f32_e32 v199, v200, v201
	v_add_f32_e32 v199, v202, v199
	v_add_f32_e32 v199, v203, v199
	ds_bpermute_b32 v156, v1, v154
	ds_bpermute_b32 v157, v1, v155
	ds_bpermute_b32 v153, v22, v152
	ds_bpermute_b32 v178, v1, v176
	ds_bpermute_b32 v179, v1, v177
	ds_bpermute_b32 v175, v22, v174
	ds_bpermute_b32 v200, v1, v198
	ds_bpermute_b32 v201, v1, v199
	ds_bpermute_b32 v197, v22, v196
	s_waitcnt lgkmcnt(0)
; DI unsigned pk_bf16(float lo, float hi) { f32x2 v = {lo, hi}; hbf16x2 r = __builtin_convertvector(v, hbf16x2); return __builtin_bit_cast(unsigned, r); }
; DI float bflo(unsigned w) { return __uint_as_float(w << 16); }
; DI float bfhi(unsigned w) { return __uint_as_float(w & 0xffff0000u); }
; DI float bf2f(bf16_t b) { return __uint_as_float(((unsigned)b) << 16); }
; DI bf16_t f2bf(float f) { return (bf16_t)(pk_bf16(f, 0.f) & 0xffffu); }
; DI void phase_l0_rows(const Params& p, int G, int bid) {
;     ...
;             ss = wave_sum(ss);
;             const float r = rsqrtf(ss * (1.0f / 512.0f) + EPS);
;             const f32x4 g0 = *(const f32x4*)(p.in[12] + 8 * lane), g1 = *(const f32x4*)(p.in[12] + 8 * lane + 4);
;             u32x4 o; o.x = pk_bf16(v[0] * r * g0[0], v[1] * r * g0[1]); o.y = pk_bf16(v[2] * r * g0[2], v[3] * r * g0[3]);
;             o.z = pk_bf16(v[4] * r * g1[0], v[5] * r * g1[1]); o.w = pk_bf16(v[6] * r * g1[2], v[7] * r * g1[3]);
;             *(u32x4*)(CQN + (size_t)row * 512 + 8 * lane) = o;
;         }
;         {
;             const u32x2 w = *(const u32x2*)(z + 512 + 4 * lane);
;             float v[4] = {bflo(w.x), bfhi(w.x), bflo(w.y), bfhi(w.y)};
;             float ss = v[0] * v[0] + v[1] * v[1] + v[2] * v[2] + v[3] * v[3];
;             ss = wave_sum(ss);
;             const float r = rsqrtf(ss * (1.0f / 256.0f) + EPS);
;             const f32x4 g = *(const f32x4*)(p.in[14] + 4 * lane);
;             u32x2 o; o.x = pk_bf16(v[0] * r * g[0], v[1] * r * g[1]); o.y = pk_bf16(v[2] * r * g[2], v[3] * r * g[3]);
;             *(u32x2*)(CKVN + (size_t)row * 256 + 4 * lane) = o;
;         }
;         {
;             const float x = bf2f(z[768 + lane]);
;             const float xp = __shfl_xor(x, 16);
;             float o = x;
;             if (row >= NCTX) {
;                 const int t = (row - NCTX) & (SEQ - 1), axis = lane >> 5, part = (lane >> 4) & 1, i = lane & 15;
;                 const int pos = axis ? (t & 63) : (t >> 6);
;                 const f32x2 cs = R0[pos * 16 + i];
;                 o = part ? (x * cs[0] + xp * cs[1]) : (x * cs[0] - xp * cs[1]);
;             }
;             KR[(size_t)row * 64 + lane] = f2bf(o);
	v_add_f32_e32 v154, v154, v156
	v_add_f32_e32 v155, v155, v157
	v_add_f32_e32 v176, v176, v178
	v_add_f32_e32 v177, v177, v179
	v_add_f32_e32 v198, v198, v200
	v_add_f32_e32 v199, v199, v201
	ds_bpermute_b32 v156, v22, v154
	ds_bpermute_b32 v157, v22, v155
	ds_bpermute_b32 v178, v22, v176
	ds_bpermute_b32 v179, v22, v177
	ds_bpermute_b32 v200, v22, v198
	ds_bpermute_b32 v201, v22, v199
	s_waitcnt lgkmcnt(0)
	v_add_f32_e32 v154, v154, v156
	v_add_f32_e32 v155, v155, v157
	v_add_f32_e32 v176, v176, v178
	v_add_f32_e32 v177, v177, v179
	v_add_f32_e32 v198, v198, v200
	v_add_f32_e32 v199, v199, v201
	ds_bpermute_b32 v156, v23, v154
	ds_bpermute_b32 v157, v23, v155
	ds_bpermute_b32 v178, v23, v176
	ds_bpermute_b32 v179, v23, v177
	ds_bpermute_b32 v200, v23, v198
	ds_bpermute_b32 v201, v23, v199
	s_waitcnt lgkmcnt(0)
	v_add_f32_e32 v154, v154, v156
	v_add_f32_e32 v155, v155, v157
	v_add_f32_e32 v176, v176, v178
	v_add_f32_e32 v177, v177, v179
	v_add_f32_e32 v198, v198, v200
	v_add_f32_e32 v199, v199, v201
	ds_bpermute_b32 v156, v24, v154
	ds_bpermute_b32 v157, v24, v155
	ds_bpermute_b32 v178, v24, v176
	ds_bpermute_b32 v179, v24, v177
	ds_bpermute_b32 v200, v24, v198
	ds_bpermute_b32 v201, v24, v199
	s_waitcnt lgkmcnt(0)
	v_add_f32_e32 v154, v154, v156
	v_add_f32_e32 v155, v155, v157
	v_add_f32_e32 v176, v176, v178
	v_add_f32_e32 v177, v177, v179
	v_add_f32_e32 v198, v198, v200
	v_add_f32_e32 v199, v199, v201
	ds_bpermute_b32 v156, v25, v154
	ds_bpermute_b32 v157, v25, v155
	ds_bpermute_b32 v178, v25, v176
	ds_bpermute_b32 v179, v25, v177
	ds_bpermute_b32 v200, v25, v198
	ds_bpermute_b32 v201, v25, v199
	s_waitcnt lgkmcnt(0)
	v_add_f32_e32 v154, v154, v156
	v_add_f32_e32 v155, v155, v157
	v_add_f32_e32 v176, v176, v178
	v_add_f32_e32 v177, v177, v179
	v_add_f32_e32 v198, v198, v200
	v_add_f32_e32 v199, v199, v201
	ds_bpermute_b32 v156, v26, v154
	ds_bpermute_b32 v157, v26, v155
	ds_bpermute_b32 v178, v26, v176
	ds_bpermute_b32 v179, v26, v177
	ds_bpermute_b32 v200, v26, v198
	ds_bpermute_b32 v201, v26, v199
	s_waitcnt lgkmcnt(0)
	v_add_f32_e32 v154, v154, v156
	v_add_f32_e32 v155, v155, v157
	v_add_f32_e32 v176, v176, v178
	v_add_f32_e32 v177, v177, v179
	v_add_f32_e32 v198, v198, v200
	v_add_f32_e32 v199, v199, v201
	s_add_i32 s18, s16, 48
	v_fmamk_f32 v154, v154, 0x3b000000, v28
	v_mul_f32_e32 v156, 0x4b800000, v154
	v_cmp_gt_f32_e32 vcc, s14, v154
	s_nop 1
	v_cndmask_b32_e32 v154, v154, v156, vcc
	v_rsq_f32_e32 v158, v154
	s_nop 0
	v_mul_f32_e32 v156, 0x45800000, v158
	s_nop 0
	v_cndmask_b32_e32 v158, v158, v156, vcc
	v_fmamk_f32 v155, v155, 0x3b800000, v28
	v_mul_f32_e32 v156, 0x4b800000, v155
	v_cmp_gt_f32_e32 vcc, s14, v155
	s_nop 1
	v_cndmask_b32_e32 v155, v155, v156, vcc
	v_rsq_f32_e32 v160, v155
	s_nop 0
	v_mul_f32_e32 v156, 0x45800000, v160
	s_nop 0
	v_cndmask_b32_e32 v160, v160, v156, vcc
	v_pk_mul_f32 v[140:141], v[158:159], v[140:141] op_sel_hi:[0,1]
	v_pk_mul_f32 v[142:143], v[158:159], v[142:143] op_sel_hi:[0,1]
	v_pk_mul_f32 v[144:145], v[158:159], v[144:145] op_sel_hi:[0,1]
	v_pk_mul_f32 v[146:147], v[158:159], v[146:147] op_sel_hi:[0,1]
	v_pk_mul_f32 v[140:141], v[34:35], v[140:141]
	v_pk_mul_f32 v[142:143], v[36:37], v[142:143]
	v_pk_mul_f32 v[144:145], v[38:39], v[144:145]
	v_pk_mul_f32 v[146:147], v[40:41], v[146:147]
	s_lshl_b32 s19, s18, 10
	s_add_u32 s19, s19, 0x2b70e000
	s_add_u32 s86, s50, s19
	s_addc_u32 s87, s51, 0
	v_cvt_pk_bf16_f32 v140, v140, v141
	v_cvt_pk_bf16_f32 v141, v142, v143
	v_cvt_pk_bf16_f32 v142, v144, v145
	v_cvt_pk_bf16_f32 v143, v146, v147
	global_store_dwordx4 v2, v[140:143], s[86:87]
	v_pk_mul_f32 v[148:149], v[160:161], v[148:149] op_sel_hi:[0,1]
	v_pk_mul_f32 v[150:151], v[160:161], v[150:151] op_sel_hi:[0,1]
	v_pk_mul_f32 v[148:149], v[42:43], v[148:149]
	v_pk_mul_f32 v[150:151], v[44:45], v[150:151]
	s_lshl_b32 s19, s18, 9
	s_add_u32 s19, s19, 0x2c00e000
	s_add_u32 s88, s50, s19
	s_addc_u32 s89, s51, 0
	v_cvt_pk_bf16_f32 v148, v148, v149
	v_cvt_pk_bf16_f32 v149, v150, v151
	global_store_dwordx2 v16, v[148:149], s[88:89]
	s_cmpk_lt_u32 s18, 0x400
	s_cbranch_scc1 .Ll0r_ns6
	v_mul_f32_e32 v153, v115, v153
	v_cndmask_b32_e64 v153, v153, -v153, s[4:5]
	v_fmac_f32_e32 v153, v114, v152
	v_mov_b32_e32 v152, v153
; DI unsigned pk_bf16(float lo, float hi) { f32x2 v = {lo, hi}; hbf16x2 r = __builtin_convertvector(v, hbf16x2); return __builtin_bit_cast(unsigned, r); }
; DI float bflo(unsigned w) { return __uint_as_float(w << 16); }
; DI float bfhi(unsigned w) { return __uint_as_float(w & 0xffff0000u); }
; DI float bf2f(bf16_t b) { return __uint_as_float(((unsigned)b) << 16); }
; DI bf16_t f2bf(float f) { return (bf16_t)(pk_bf16(f, 0.f) & 0xffffu); }
; DI void phase_l0_rows(const Params& p, int G, int bid) {
;     ...
;             const float r = rsqrtf(ss * (1.0f / 512.0f) + EPS);
;             const f32x4 g0 = *(const f32x4*)(p.in[12] + 8 * lane), g1 = *(const f32x4*)(p.in[12] + 8 * lane + 4);
;             u32x4 o; o.x = pk_bf16(v[0] * r * g0[0], v[1] * r * g0[1]); o.y = pk_bf16(v[2] * r * g0[2], v[3] * r * g0[3]);
;             o.z = pk_bf16(v[4] * r * g1[0], v[5] * r * g1[1]); o.w = pk_bf16(v[6] * r * g1[2], v[7] * r * g1[3]);
;             *(u32x4*)(CQN + (size_t)row * 512 + 8 * lane) = o;
;         }
;         {
;             const u32x2 w = *(const u32x2*)(z + 512 + 4 * lane);
;             float v[4] = {bflo(w.x), bfhi(w.x), bflo(w.y), bfhi(w.y)};
;             float ss = v[0] * v[0] + v[1] * v[1] + v[2] * v[2] + v[3] * v[3];
;             ss = wave_sum(ss);
;             const float r = rsqrtf(ss * (1.0f / 256.0f) + EPS);
;             const f32x4 g = *(const f32x4*)(p.in[14] + 4 * lane);
;             u32x2 o; o.x = pk_bf16(v[0] * r * g[0], v[1] * r * g[1]); o.y = pk_bf16(v[2] * r * g[2], v[3] * r * g[3]);
;             *(u32x2*)(CKVN + (size_t)row * 256 + 4 * lane) = o;
;         }
;         {
;             const float x = bf2f(z[768 + lane]);
;             const float xp = __shfl_xor(x, 16);
;             float o = x;
;             if (row >= NCTX) {
;                 const int t = (row - NCTX) & (SEQ - 1), axis = lane >> 5, part = (lane >> 4) & 1, i = lane & 15;
;                 const int pos = axis ? (t & 63) : (t >> 6);
;                 const f32x2 cs = R0[pos * 16 + i];
;                 o = part ? (x * cs[0] + xp * cs[1]) : (x * cs[0] - xp * cs[1]);
;             }
;             KR[(size_t)row * 64 + lane] = f2bf(o);
.Ll0r_ns6:
	s_lshl_b32 s19, s18, 7
	s_add_u32 s19, s19, 0x2c48e000
	s_add_u32 s90, s50, s19
	s_addc_u32 s91, s51, 0
	v_cvt_pk_bf16_f32 v152, v152, v152
	global_store_short v18, v152, s[90:91]
	s_add_i32 s18, s16, 56
	v_fmamk_f32 v176, v176, 0x3b000000, v28
	v_mul_f32_e32 v178, 0x4b800000, v176
	v_cmp_gt_f32_e32 vcc, s14, v176
	s_nop 1
	v_cndmask_b32_e32 v176, v176, v178, vcc
	v_rsq_f32_e32 v180, v176
	s_nop 0
	v_mul_f32_e32 v178, 0x45800000, v180
	s_nop 0
	v_cndmask_b32_e32 v180, v180, v178, vcc
	v_fmamk_f32 v177, v177, 0x3b800000, v28
	v_mul_f32_e32 v178, 0x4b800000, v177
	v_cmp_gt_f32_e32 vcc, s14, v177
	s_nop 1
	v_cndmask_b32_e32 v177, v177, v178, vcc
	v_rsq_f32_e32 v182, v177
	s_nop 0
	v_mul_f32_e32 v178, 0x45800000, v182
	s_nop 0
	v_cndmask_b32_e32 v182, v182, v178, vcc
	v_pk_mul_f32 v[162:163], v[180:181], v[162:163] op_sel_hi:[0,1]
	v_pk_mul_f32 v[164:165], v[180:181], v[164:165] op_sel_hi:[0,1]
	v_pk_mul_f32 v[166:167], v[180:181], v[166:167] op_sel_hi:[0,1]
	v_pk_mul_f32 v[168:169], v[180:181], v[168:169] op_sel_hi:[0,1]
	v_pk_mul_f32 v[162:163], v[34:35], v[162:163]
	v_pk_mul_f32 v[164:165], v[36:37], v[164:165]
	v_pk_mul_f32 v[166:167], v[38:39], v[166:167]
	v_pk_mul_f32 v[168:169], v[40:41], v[168:169]
	s_lshl_b32 s19, s18, 10
	s_add_u32 s19, s19, 0x2b70e000
	s_add_u32 s86, s50, s19
	s_addc_u32 s87, s51, 0
	v_cvt_pk_bf16_f32 v162, v162, v163
	v_cvt_pk_bf16_f32 v163, v164, v165
	v_cvt_pk_bf16_f32 v164, v166, v167
	v_cvt_pk_bf16_f32 v165, v168, v169
	global_store_dwordx4 v2, v[162:165], s[86:87]
	v_pk_mul_f32 v[170:171], v[182:183], v[170:171] op_sel_hi:[0,1]
	v_pk_mul_f32 v[172:173], v[182:183], v[172:173] op_sel_hi:[0,1]
	v_pk_mul_f32 v[170:171], v[42:43], v[170:171]
	v_pk_mul_f32 v[172:173], v[44:45], v[172:173]
	s_lshl_b32 s19, s18, 9
	s_add_u32 s19, s19, 0x2c00e000
	s_add_u32 s88, s50, s19
	s_addc_u32 s89, s51, 0
	v_cvt_pk_bf16_f32 v170, v170, v171
	v_cvt_pk_bf16_f32 v171, v172, v173
	global_store_dwordx2 v16, v[170:171], s[88:89]
	s_cmpk_lt_u32 s18, 0x400
	s_cbranch_scc1 .Ll0r_ns7
	v_mul_f32_e32 v175, v125, v175
	v_cndmask_b32_e64 v175, v175, -v175, s[4:5]
	v_fmac_f32_e32 v175, v124, v174
	v_mov_b32_e32 v174, v175
.Ll0r_ns7:
	s_lshl_b32 s19, s18, 7
	s_add_u32 s19, s19, 0x2c48e000
	s_add_u32 s90, s50, s19
	s_addc_u32 s91, s51, 0
	v_cvt_pk_bf16_f32 v174, v174, v174
	global_store_short v18, v174, s[90:91]
	s_add_i32 s18, s16, 64
	v_fmamk_f32 v198, v198, 0x3b000000, v28
	v_mul_f32_e32 v200, 0x4b800000, v198
	v_cmp_gt_f32_e32 vcc, s14, v198
	s_nop 1
	v_cndmask_b32_e32 v198, v198, v200, vcc
	v_rsq_f32_e32 v202, v198
	s_nop 0
	v_mul_f32_e32 v200, 0x45800000, v202
	s_nop 0
	v_cndmask_b32_e32 v202, v202, v200, vcc
	v_fmamk_f32 v199, v199, 0x3b800000, v28
	v_mul_f32_e32 v200, 0x4b800000, v199
	v_cmp_gt_f32_e32 vcc, s14, v199
	s_nop 1
	v_cndmask_b32_e32 v199, v199, v200, vcc
	v_rsq_f32_e32 v204, v199
	s_nop 0
	v_mul_f32_e32 v200, 0x45800000, v204
	s_nop 0
	v_cndmask_b32_e32 v204, v204, v200, vcc
	v_pk_mul_f32 v[184:185], v[202:203], v[184:185] op_sel_hi:[0,1]
	v_pk_mul_f32 v[186:187], v[202:203], v[186:187] op_sel_hi:[0,1]
	v_pk_mul_f32 v[188:189], v[202:203], v[188:189] op_sel_hi:[0,1]
	v_pk_mul_f32 v[190:191], v[202:203], v[190:191] op_sel_hi:[0,1]
	v_pk_mul_f32 v[184:185], v[34:35], v[184:185]
	v_pk_mul_f32 v[186:187], v[36:37], v[186:187]
	v_pk_mul_f32 v[188:189], v[38:39], v[188:189]
	v_pk_mul_f32 v[190:191], v[40:41], v[190:191]
	s_lshl_b32 s19, s18, 10
	s_add_u32 s19, s19, 0x2b70e000
	s_add_u32 s86, s50, s19
	s_addc_u32 s87, s51, 0
	v_cvt_pk_bf16_f32 v184, v184, v185
	v_cvt_pk_bf16_f32 v185, v186, v187
	v_cvt_pk_bf16_f32 v186, v188, v189
	v_cvt_pk_bf16_f32 v187, v190, v191
	global_store_dwordx4 v2, v[184:187], s[86:87]
	v_pk_mul_f32 v[192:193], v[204:205], v[192:193] op_sel_hi:[0,1]
	v_pk_mul_f32 v[194:195], v[204:205], v[194:195] op_sel_hi:[0,1]
	v_pk_mul_f32 v[192:193], v[42:43], v[192:193]
	v_pk_mul_f32 v[194:195], v[44:45], v[194:195]
	s_lshl_b32 s19, s18, 9
	s_add_u32 s19, s19, 0x2c00e000
	s_add_u32 s88, s50, s19
	s_addc_u32 s89, s51, 0
	v_cvt_pk_bf16_f32 v192, v192, v193
	v_cvt_pk_bf16_f32 v193, v194, v195
	global_store_dwordx2 v16, v[192:193], s[88:89]
	s_cmpk_lt_u32 s18, 0x400
	s_cbranch_scc1 .Ll0r_ns8
	v_mul_f32_e32 v197, v135, v197
	v_cndmask_b32_e64 v197, v197, -v197, s[4:5]
	v_fmac_f32_e32 v197, v134, v196
	v_mov_b32_e32 v196, v197
.Ll0r_ns8:
	s_lshl_b32 s19, s18, 7
	s_add_u32 s19, s19, 0x2c48e000
	s_add_u32 s90, s50, s19
	s_addc_u32 s91, s51, 0
	v_cvt_pk_bf16_f32 v196, v196, v196
	global_store_short v18, v196, s[90:91]
	s_branch .LBB0_336
